# P0 meta K/V projection: prefetch block touches the thread's 56 later weight rows before the 8-trip loop (trips 1..7 hit L2); m1
# baseline (speedup 1.0000x reference)
; #define LAS __attribute__((address_space(3)))
; __device__ __forceinline__ void phase0(const Args& a, LAS unsigned char* lds, int vcu, int G, int tid, int lane, int wave) {
;     unsigned char* ws = a.ws;
;     for (int unit = vcu; unit < 256; unit += G) {
;         LAS float* um = (LAS float*)lds;
;         for (int rr = 0; rr < 2; ++rr) { const int r = wave * 2 + rr;
;             const f32x4* xr = (const f32x4*)(a.in[I_META] + (size_t)r * DM) + lane; const f32x4* gr = (const f32x4*)a.in[I_GMIX] + lane;
;             f32x4 v[8]; float s = 0.f;
; #pragma unroll
;             for (int j = 0; j < 8; ++j) { v[j] = xr[64 * j]; s += (v[j].x * v[j].x + v[j].y * v[j].y) + (v[j].z * v[j].z + v[j].w * v[j].w); }
;             const float rstd = 1.0f / sqrtf(wave_sum(s) * (1.f / DM) + RMS_EPS);
.LBB0_16:
	global_load_dwordx4 v[2:5], v[72:73], off offset:2048
	global_load_dwordx4 v[6:9], v[76:77], off
	global_load_dwordx4 v[10:13], v[82:83], off offset:2048
	global_load_dwordx4 v[38:41], v[72:73], off
	global_load_dwordx4 v[22:25], v[72:73], off offset:1024
	global_load_dwordx4 v[42:45], v[82:83], off
	global_load_dwordx4 v[34:37], v[82:83], off offset:1024
	global_load_dwordx4 v[26:29], v[72:73], off offset:3072
	global_load_dwordx4 v[30:33], v[74:75], off
	global_load_dwordx4 v[18:21], v[78:79], off
	global_load_dwordx4 v[14:17], v[80:81], off
	global_load_dwordx4 v[46:49], v[84:85], off
	global_load_dwordx4 v[50:53], v[82:83], off offset:3072
	global_load_dwordx4 v[54:57], v[86:87], off
	global_load_dwordx4 v[58:61], v[90:91], off
	global_load_dwordx4 v[66:69], v[132:133], off
	global_load_dwordx4 v[62:65], v[88:89], off
	s_and_b32 s8, s61, 0x3f0
	s_ashr_i32 s9, s64, 6
	s_cmp_eq_u32 s9, 2
	s_movk_i32 s14, 0x1000
	s_waitcnt vmcnt(16)
	v_pk_mul_f32 v[112:113], v[4:5], v[4:5]
	v_pk_mul_f32 v[114:115], v[2:3], v[2:3]
	s_waitcnt vmcnt(15)
	v_pk_mul_f32 v[116:117], v[8:9], v[8:9]
	v_pk_mul_f32 v[118:119], v[6:7], v[6:7]
	s_waitcnt vmcnt(13)
	v_mov_b32_e32 v126, v39
	s_waitcnt vmcnt(12)
	v_mov_b32_e32 v127, v23
	v_mov_b32_e32 v124, v38
	v_mov_b32_e32 v125, v22
	v_mov_b32_e32 v142, v41
	v_mov_b32_e32 v143, v25
	v_pk_mov_b32 v[158:159], v[114:115], v[112:113] op_sel:[1,0]
	v_mov_b32_e32 v115, v113
	v_pk_mov_b32 v[112:113], v[118:119], v[116:117] op_sel:[1,0]
	v_mov_b32_e32 v119, v117
	v_pk_mul_f32 v[116:117], v[126:127], v[126:127]
	v_mov_b32_e32 v128, v40
	v_mov_b32_e32 v129, v24
	v_pk_fma_f32 v[116:117], v[124:125], v[124:125], v[116:117]
	v_pk_mul_f32 v[124:125], v[142:143], v[142:143]
	s_waitcnt vmcnt(9)
	v_mul_f32_e32 v70, v27, v27
	v_pk_fma_f32 v[124:125], v[128:129], v[128:129], v[124:125]
	v_mul_f32_e32 v152, v29, v29
	s_waitcnt vmcnt(8)
	v_mul_f32_e32 v153, v33, v33
	v_pk_add_f32 v[114:115], v[158:159], v[114:115]
	v_pk_add_f32 v[116:117], v[116:117], v[124:125]
	v_mul_f32_e32 v131, v32, v32
	v_mul_f32_e32 v162, v31, v31
	v_mul_f32_e32 v163, v30, v30
	v_pk_fma_f32 v[128:129], v[26:27], v[26:27], v[70:71] op_sel_hi:[1,1,0]
	v_pk_fma_f32 v[142:143], v[28:29], v[28:29], v[152:153] op_sel_hi:[1,1,0]
	v_pk_add_f32 v[114:115], v[114:115], v[114:115] op_sel:[0,1] op_sel_hi:[1,0]
	v_pk_add_f32 v[116:117], v[116:117], v[116:117] op_sel:[0,1] op_sel_hi:[1,0]
	v_mov_b32_e32 v129, v131
	v_mov_b32_e32 v143, v153
	v_mov_b32_e32 v115, v162
	v_mov_b32_e32 v117, v163
	v_pk_add_f32 v[124:125], v[128:129], v[142:143]
	v_pk_add_f32 v[114:115], v[116:117], v[114:115]
	s_waitcnt vmcnt(7)
	v_mul_f32_e32 v154, v19, v19
	v_mul_f32_e32 v156, v21, v21
	v_pk_add_f32 v[112:113], v[112:113], v[118:119]
	v_pk_add_f32 v[114:115], v[114:115], v[124:125]
	s_waitcnt vmcnt(6)
	v_mul_f32_e32 v160, v16, v16
	v_mul_f32_e32 v161, v17, v17
	v_mul_f32_e32 v164, v15, v15
	v_mul_f32_e32 v165, v14, v14
	v_pk_fma_f32 v[154:155], v[18:19], v[18:19], v[154:155] op_sel_hi:[1,1,0]
	v_pk_fma_f32 v[156:157], v[20:21], v[20:21], v[156:157] op_sel_hi:[1,1,0]
	v_pk_add_f32 v[112:113], v[112:113], v[112:113] op_sel:[0,1] op_sel_hi:[1,0]
	v_pk_add_f32 v[114:115], v[114:115], v[114:115] op_sel:[0,1] op_sel_hi:[1,0]
	v_mov_b32_e32 v155, v160
	v_mov_b32_e32 v157, v161
	v_mov_b32_e32 v113, v164
	v_mov_b32_e32 v115, v165
	v_pk_add_f32 v[128:129], v[154:155], v[156:157]
	v_pk_add_f32 v[112:113], v[114:115], v[112:113]
	s_waitcnt vmcnt(4)
	v_mul_f32_e32 v118, v53, v53
	v_pk_add_f32 v[112:113], v[112:113], v[128:129]
	v_pk_fma_f32 v[118:119], v[52:53], v[52:53], v[118:119] op_sel_hi:[1,1,0]
	v_add_f32_e32 v70, v112, v113
	ds_bpermute_b32 v116, v102, v70
	v_pk_mul_f32 v[120:121], v[12:13], v[12:13]
	v_pk_mul_f32 v[122:123], v[10:11], v[10:11]
	v_mul_f32_e32 v126, v51, v51
	v_pk_mov_b32 v[114:115], v[122:123], v[120:121] op_sel:[1,0]
	s_waitcnt lgkmcnt(0)
	v_add_f32_e32 v70, v70, v116
	ds_bpermute_b32 v127, v103, v70
	v_mov_b32_e32 v123, v121
	v_pk_add_f32 v[114:115], v[114:115], v[122:123]
	s_waitcnt vmcnt(3)
	v_pk_mul_f32 v[152:153], v[56:57], v[56:57]
	v_pk_mul_f32 v[112:113], v[54:55], v[54:55]
	s_waitcnt lgkmcnt(0)
	v_add_f32_e32 v70, v70, v127
	ds_bpermute_b32 v119, v104, v70
	v_pk_fma_f32 v[124:125], v[50:51], v[50:51], v[126:127] op_sel_hi:[1,1,0]
	v_pk_mov_b32 v[126:127], v[112:113], v[152:153] op_sel:[1,0]
	v_mov_b32_e32 v113, v153
	v_pk_add_f32 v[112:113], v[126:127], v[112:113]
	s_waitcnt lgkmcnt(0)
	v_add_f32_e32 v70, v70, v119
	ds_bpermute_b32 v129, v105, v70
	v_pk_add_f32 v[112:113], v[112:113], v[112:113] op_sel:[0,1] op_sel_hi:[1,0]
	v_mov_b32_e32 v146, v43
	v_mov_b32_e32 v147, v35
	v_mov_b32_e32 v150, v45
	s_waitcnt lgkmcnt(0)
	v_add_f32_e32 v70, v70, v129
	ds_bpermute_b32 v122, v106, v70
	v_mov_b32_e32 v151, v37
	v_mov_b32_e32 v144, v42
	v_mov_b32_e32 v145, v34
	v_mov_b32_e32 v148, v44
	s_waitcnt lgkmcnt(0)
	v_add_f32_e32 v70, v70, v122
	ds_bpermute_b32 v113, v107, v70
	v_mov_b32_e32 v149, v36
	v_pk_mul_f32 v[116:117], v[146:147], v[146:147]
	v_pk_mul_f32 v[120:121], v[150:151], v[150:151]
	v_pk_fma_f32 v[116:117], v[144:145], v[144:145], v[116:117]
	s_waitcnt lgkmcnt(0)
	v_add_f32_e32 v70, v70, v113
	v_fmamk_f32 v70, v70, 0x3a000000, v108
	v_pk_fma_f32 v[120:121], v[148:149], v[148:149], v[120:121]
	v_mul_f32_e32 v113, 0x4f800000, v70
	v_cmp_gt_f32_e32 vcc, s63, v70
	v_pk_add_f32 v[116:117], v[116:117], v[120:121]
	v_mul_f32_e32 v166, v46, v46
	v_cndmask_b32_e32 v120, v70, v113, vcc
	v_sqrt_f32_e32 v121, v120
	v_mul_f32_e32 v167, v47, v47
	v_mul_f32_e32 v158, v48, v48
	v_mul_f32_e32 v159, v49, v49
	v_pk_add_f32 v[114:115], v[114:115], v[114:115] op_sel:[0,1] op_sel_hi:[1,0]
	v_pk_add_f32 v[116:117], v[116:117], v[116:117] op_sel:[0,1] op_sel_hi:[1,0]
	v_mov_b32_e32 v125, v158
	v_mov_b32_e32 v119, v159
	v_mov_b32_e32 v115, v167
	v_mov_b32_e32 v117, v166
	v_pk_add_f32 v[118:119], v[124:125], v[118:119]
	v_pk_add_f32 v[114:115], v[116:117], v[114:115]
	v_add_u32_e32 v70, -1, v121
	v_pk_add_f32 v[114:115], v[114:115], v[118:119]
	v_fma_f32 v113, -v70, v121, v120
	s_waitcnt vmcnt(2)
; #define LAS __attribute__((address_space(3)))
; __device__ __forceinline__ float wave_sum(float v) {
; #pragma unroll
;     for (int o = 1; o < 64; o <<= 1) v += __shfl_xor(v, o);
;     return v;
; }
; __device__ __forceinline__ void phase0(const Args& a, LAS unsigned char* lds, int vcu, int G, int tid, int lane, int wave) {
;     ...
;         for (int rr = 0; rr < 2; ++rr) { const int r = wave * 2 + rr;
;             const f32x4* xr = (const f32x4*)(a.in[I_META] + (size_t)r * DM) + lane; const f32x4* gr = (const f32x4*)a.in[I_GMIX] + lane;
;             f32x4 v[8]; float s = 0.f;
; #pragma unroll
;             for (int j = 0; j < 8; ++j) { v[j] = xr[64 * j]; s += (v[j].x * v[j].x + v[j].y * v[j].y) + (v[j].z * v[j].z + v[j].w * v[j].w); }
;             const float rstd = 1.0f / sqrtf(wave_sum(s) * (1.f / DM) + RMS_EPS);
; #pragma unroll
;             for (int j = 0; j < 8; ++j) { const f32x4 gg = gr[64 * j]; *(LAS f32x4*)(um + r * DM + 4 * (lane + 64 * j)) = v[j] * rstd * gg; } }
	v_mul_f32_e32 v128, v58, v58
	v_pk_add_f32 v[114:115], v[114:115], v[114:115] op_sel:[0,1] op_sel_hi:[1,0]
	v_cmp_ge_f32_e64 s[6:7], 0, v113
	v_mov_b32_e32 v115, v128
	v_mul_f32_e32 v113, v59, v59
	v_cndmask_b32_e64 v118, v121, v70, s[6:7]
	s_waitcnt vmcnt(0)
	v_mul_f32_e32 v70, v63, v63
	v_pk_add_f32 v[112:113], v[114:115], v[112:113]
	v_pk_fma_f32 v[114:115], v[62:63], v[62:63], v[70:71] op_sel_hi:[1,1,0]
	v_mul_f32_e32 v70, v65, v65
	v_pk_fma_f32 v[116:117], v[64:65], v[64:65], v[70:71] op_sel_hi:[1,1,0]
	v_mul_f32_e32 v115, v60, v60
	v_mul_f32_e32 v117, v61, v61
	v_pk_add_f32 v[114:115], v[114:115], v[116:117]
	v_add_u32_e32 v117, 1, v121
	v_pk_add_f32 v[112:113], v[112:113], v[114:115]
	s_nop 0
	v_add_f32_e32 v70, v112, v113
	ds_bpermute_b32 v116, v102, v70
	v_fma_f32 v112, -v117, v121, v120
	v_cmp_lt_f32_e64 s[6:7], 0, v112
	global_load_dwordx4 v[112:115], v[132:133], off offset:1024
	s_waitcnt lgkmcnt(0)
	v_add_f32_e32 v70, v70, v116
	ds_bpermute_b32 v116, v103, v70
	v_cndmask_b32_e64 v117, v118, v117, s[6:7]
	v_mul_f32_e32 v118, 0x37800000, v117
	v_cndmask_b32_e32 v121, v117, v118, vcc
	v_cmp_class_f32_e32 vcc, v120, v109
	s_waitcnt lgkmcnt(0)
	v_add_f32_e32 v70, v70, v116
	ds_bpermute_b32 v122, v104, v70
	v_cndmask_b32_e32 v128, v121, v120, vcc
	v_div_scale_f32 v129, s[6:7], v128, v128, 1.0
	v_rcp_f32_e32 v131, v129
	s_waitcnt lgkmcnt(0)
	v_add_f32_e32 v70, v70, v122
	ds_bpermute_b32 v124, v105, v70
	v_div_scale_f32 v143, vcc, 1.0, v128, 1.0
	v_fma_f32 v125, -v129, v131, 1.0
	v_fmac_f32_e32 v131, v125, v131
	s_waitcnt lgkmcnt(0)
	v_add_f32_e32 v70, v70, v124
	ds_bpermute_b32 v142, v106, v70
	v_mul_f32_e32 v146, v143, v131
	global_load_dwordx4 v[116:119], v[132:133], off offset:2048
	global_load_dwordx4 v[120:123], v[132:133], off offset:3072
	global_load_dwordx4 v[124:127], v[134:135], off
	s_waitcnt lgkmcnt(0)
	v_add_f32_e32 v70, v70, v142
	ds_bpermute_b32 v147, v107, v70
	v_fma_f32 v142, -v129, v146, v143
	v_fmac_f32_e32 v146, v142, v131
	v_fma_f32 v129, -v129, v146, v143
	global_load_dwordx4 v[142:145], v[136:137], off
	s_waitcnt lgkmcnt(0)
	v_add_f32_e32 v70, v70, v147
	v_fmamk_f32 v70, v70, 0x3a000000, v108
	v_mul_f32_e32 v147, 0x4f800000, v70
	v_cmp_gt_f32_e64 s[6:7], s63, v70
	s_nop 1
	v_cndmask_b32_e64 v154, v70, v147, s[6:7]
	v_sqrt_f32_e32 v150, v154
	v_div_fmas_f32 v70, v129, v131, v146
	v_div_fixup_f32 v70, v70, v128, 1.0
	global_load_dwordx4 v[146:149], v[138:139], off
	v_add_u32_e32 v128, -1, v150
	v_fma_f32 v129, -v128, v150, v154
	v_cmp_ge_f32_e32 vcc, 0, v129
	v_add_u32_e32 v129, 1, v150
	v_fma_f32 v131, -v129, v150, v154
	v_cndmask_b32_e32 v128, v150, v128, vcc
	global_load_dwordx4 v[150:153], v[140:141], off
	v_cmp_lt_f32_e32 vcc, 0, v131
	v_pk_mul_f32 v[38:39], v[38:39], v[70:71] op_sel_hi:[1,0]
	v_pk_mul_f32 v[40:41], v[40:41], v[70:71] op_sel_hi:[1,0]
	v_cndmask_b32_e32 v128, v128, v129, vcc
	v_mul_f32_e32 v129, 0x37800000, v128
	v_cndmask_b32_e64 v128, v128, v129, s[6:7]
	v_cmp_class_f32_e32 vcc, v154, v109
	v_pk_mul_f32 v[2:3], v[2:3], v[70:71] op_sel_hi:[1,0]
	v_pk_mul_f32 v[4:5], v[4:5], v[70:71] op_sel_hi:[1,0]
	v_cndmask_b32_e32 v128, v128, v154, vcc
	v_div_scale_f32 v129, s[6:7], v128, v128, 1.0
	v_rcp_f32_e32 v131, v129
	v_pk_mul_f32 v[40:41], v[68:69], v[40:41]
	v_pk_mul_f32 v[38:39], v[66:67], v[38:39]
	v_pk_mul_f32 v[22:23], v[22:23], v[70:71] op_sel_hi:[1,0]
	v_fma_f32 v154, -v129, v131, 1.0
	v_fmac_f32_e32 v131, v154, v131
	v_div_scale_f32 v154, vcc, 1.0, v128, 1.0
	v_mul_f32_e32 v155, v154, v131
	v_fma_f32 v156, -v129, v155, v154
	v_fmac_f32_e32 v155, v156, v131
	v_fma_f32 v129, -v129, v155, v154
	v_div_fmas_f32 v129, v129, v131, v155
	v_div_fixup_f32 v128, v129, v128, 1.0
	v_pk_mul_f32 v[42:43], v[42:43], v[128:129] op_sel_hi:[1,0]
	v_pk_mul_f32 v[24:25], v[24:25], v[70:71] op_sel_hi:[1,0]
	v_pk_mul_f32 v[42:43], v[66:67], v[42:43]
	v_pk_mul_f32 v[26:27], v[26:27], v[70:71] op_sel_hi:[1,0]
	v_pk_mul_f32 v[28:29], v[28:29], v[70:71] op_sel_hi:[1,0]
	v_pk_mul_f32 v[32:33], v[32:33], v[70:71] op_sel_hi:[1,0]
	v_pk_mul_f32 v[30:31], v[30:31], v[70:71] op_sel_hi:[1,0]
	v_pk_mul_f32 v[8:9], v[8:9], v[70:71] op_sel_hi:[1,0]
	v_pk_mul_f32 v[6:7], v[6:7], v[70:71] op_sel_hi:[1,0]
	v_add_u32_e32 v66, s33, v130
	s_cselect_b64 s[6:7], -1, 0
	s_waitcnt vmcnt(6)
	v_pk_mul_f32 v[24:25], v[114:115], v[24:25]
	v_pk_mul_f32 v[22:23], v[112:113], v[22:23]
	s_and_b64 s[26:27], s[6:7], exec
	s_cselect_b32 s14, s14, 0x1400
	s_cmp_eq_u32 s9, 1
	s_cselect_b64 s[26:27], -1, 0
	s_and_b64 s[28:29], s[26:27], exec
	v_pk_mul_f32 v[44:45], v[44:45], v[128:129] op_sel_hi:[1,0]
	s_cselect_b32 s9, 0x800, s14
	s_cmp_lt_u32 s64, 64
	v_pk_mul_f32 v[44:45], v[68:69], v[44:45]
	v_pk_mul_f32 v[34:35], v[34:35], v[128:129] op_sel_hi:[1,0]
	v_pk_mul_f32 v[36:37], v[36:37], v[128:129] op_sel_hi:[1,0]
	v_pk_mul_f32 v[10:11], v[10:11], v[128:129] op_sel_hi:[1,0]
	v_pk_mul_f32 v[12:13], v[12:13], v[128:129] op_sel_hi:[1,0]
	v_pk_mul_f32 v[50:51], v[50:51], v[128:129] op_sel_hi:[1,0]
	s_waitcnt vmcnt(5)
	v_pk_mul_f32 v[4:5], v[118:119], v[4:5]
	v_pk_mul_f32 v[2:3], v[116:117], v[2:3]
	s_waitcnt vmcnt(4)
	v_pk_mul_f32 v[28:29], v[122:123], v[28:29]
	v_pk_mul_f32 v[26:27], v[120:121], v[26:27]
	s_waitcnt vmcnt(3)
	v_pk_mul_f32 v[30:31], v[124:125], v[30:31]
	v_pk_mul_f32 v[32:33], v[126:127], v[32:33]
	v_pk_mul_f32 v[52:53], v[52:53], v[128:129] op_sel_hi:[1,0]
	v_pk_mul_f32 v[46:47], v[46:47], v[128:129] op_sel_hi:[1,0]
	s_waitcnt vmcnt(2)
; #define LAS __attribute__((address_space(3)))
; __device__ __forceinline__ void phase0(const Args& a, LAS unsigned char* lds, int vcu, int G, int tid, int lane, int wave) {
;     ...
;             for (int j = 0; j < 8; ++j) { const f32x4 gg = gr[64 * j]; *(LAS f32x4*)(um + r * DM + 4 * (lane + 64 * j)) = v[j] * rstd * gg; } }
;         __syncthreads();
;         const int grp = unit >> 6, cbase = (unit & 63) * 16;
;         const int cl = tid & 15, ks = tid >> 4;
;         const int scol = (grp == 0 ? 1024 : grp == 1 ? 2048 : grp == 2 ? 4096 : 5120) + cbase + cl;
;         float acc[16];
; #pragma unroll
;         for (int r = 0; r < 16; ++r) acc[r] = 0.f;
;         const float* wp = a.in[I_WIN] + (size_t)(ks * 64) * INCOLS + scol;
	v_pk_mul_f32 v[6:7], v[142:143], v[6:7]
	v_pk_mul_f32 v[8:9], v[144:145], v[8:9]
	ds_write_b128 v66, v[38:41]
	ds_write_b128 v66, v[22:25] offset:1024
	ds_write_b128 v66, v[2:5] offset:2048
	ds_write_b128 v66, v[26:29] offset:3072
	ds_write_b128 v66, v[30:33] offset:4096
	ds_write_b128 v66, v[6:9] offset:5120
	v_pk_mul_f32 v[4:5], v[20:21], v[70:71] op_sel_hi:[1,0]
	v_pk_mul_f32 v[2:3], v[18:19], v[70:71] op_sel_hi:[1,0]
	v_pk_mul_f32 v[6:7], v[64:65], v[128:129] op_sel_hi:[1,0]
	v_pk_mul_f32 v[48:49], v[48:49], v[128:129] op_sel_hi:[1,0]
	s_cselect_b64 s[28:29], -1, 0
	v_pk_mul_f32 v[36:37], v[114:115], v[36:37]
	v_pk_mul_f32 v[34:35], v[112:113], v[34:35]
	v_pk_mul_f32 v[12:13], v[118:119], v[12:13]
	s_waitcnt vmcnt(1)
	v_pk_mul_f32 v[2:3], v[2:3], v[146:147]
	v_pk_mul_f32 v[4:5], v[4:5], v[148:149]
	ds_write_b128 v66, v[2:5] offset:6144
	v_pk_mul_f32 v[4:5], v[16:17], v[70:71] op_sel_hi:[1,0]
	v_pk_mul_f32 v[2:3], v[14:15], v[70:71] op_sel_hi:[1,0]
	v_pk_mul_f32 v[6:7], v[148:149], v[6:7]
	v_pk_mul_f32 v[10:11], v[116:117], v[10:11]
	s_waitcnt vmcnt(0)
	v_pk_mul_f32 v[2:3], v[2:3], v[150:151]
	v_pk_mul_f32 v[4:5], v[4:5], v[152:153]
	ds_write_b128 v66, v[2:5] offset:7168
	v_pk_mul_f32 v[4:5], v[62:63], v[128:129] op_sel_hi:[1,0]
	v_add_u32_e32 v3, s60, v130
	v_pk_mul_f32 v[4:5], v[146:147], v[4:5]
	v_pk_mul_f32 v[52:53], v[122:123], v[52:53]
	v_pk_mul_f32 v[50:51], v[120:121], v[50:51]
	v_pk_mul_f32 v[48:49], v[126:127], v[48:49]
	v_pk_mul_f32 v[46:47], v[124:125], v[46:47]
	v_pk_mul_f32 v[54:55], v[54:55], v[128:129] op_sel_hi:[1,0]
	v_pk_mul_f32 v[56:57], v[56:57], v[128:129] op_sel_hi:[1,0]
	ds_write_b128 v3, v[42:45]
	ds_write_b128 v3, v[34:37] offset:1024
	ds_write_b128 v3, v[10:13] offset:2048
	ds_write_b128 v3, v[50:53] offset:3072
	ds_write_b128 v3, v[46:49] offset:4096
	ds_write_b128 v3, v[4:7] offset:6144
	v_pk_mul_f32 v[4:5], v[58:59], v[128:129] op_sel_hi:[1,0]
	v_pk_mul_f32 v[6:7], v[60:61], v[128:129] op_sel_hi:[1,0]
	s_and_b64 s[30:31], s[28:29], exec
	v_pk_mul_f32 v[56:57], v[144:145], v[56:57]
	v_pk_mul_f32 v[54:55], v[142:143], v[54:55]
	v_pk_mul_f32 v[6:7], v[152:153], v[6:7]
	v_pk_mul_f32 v[4:5], v[150:151], v[4:5]
	s_cselect_b32 s9, 0x400, s9
	ds_write_b128 v3, v[54:57] offset:5120
	ds_write_b128 v3, v[4:7] offset:7168
	v_or_b32_e32 v3, s9, v95
	v_or_b32_e32 v3, s8, v3
	v_mov_b32_e32 v2, 0
	v_lshlrev_b32_e32 v70, 2, v3
	v_lshl_add_u64 v[4:5], v[92:93], 0, v[70:71]
	s_mov_b32 s30, 0
	v_mov_b32_e32 v3, v2
	v_mov_b32_e32 v6, v2
	v_mov_b32_e32 v7, v2
	v_mov_b32_e32 v8, v2
	v_mov_b32_e32 v9, v2
	v_mov_b32_e32 v10, v2
	v_mov_b32_e32 v11, v2
	v_mov_b32_e32 v12, v2
	v_mov_b32_e32 v13, v2
	v_mov_b32_e32 v14, v2
	v_mov_b32_e32 v15, v2
	v_mov_b32_e32 v16, v2
	v_mov_b32_e32 v17, v2
	v_mov_b32_e32 v18, v2
	v_mov_b32_e32 v19, v2
	s_waitcnt lgkmcnt(0)
	s_barrier
; __device__ __forceinline__ void phase0(const Args& a, LAS unsigned char* lds, int vcu, int G, int tid, int lane, int wave) {
;     ...
;         const float* wp = a.in[I_WIN] + (size_t)(ks * 64) * INCOLS + scol;
; #pragma unroll 1
;         for (int kb = 0; kb < 8; ++kb) { float w[8];
; #pragma unroll
;             for (int q = 0; q < 8; ++q) w[q] = wp[(size_t)(kb * 8 + q) * INCOLS];
	s_mov_b64 s[98:99], 0x6000
	v_mov_b32_e32 v248, v4
	v_mov_b32_e32 v249, v5
	v_lshl_add_u64 v[248:249], v[248:249], 0, s[98:99]
	global_load_dword v250, v[248:249], off
	v_lshl_add_u64 v[248:249], v[248:249], 0, s[98:99]
	global_load_dword v250, v[248:249], off
	v_lshl_add_u64 v[248:249], v[248:249], 0, s[98:99]
	global_load_dword v250, v[248:249], off
	v_lshl_add_u64 v[248:249], v[248:249], 0, s[98:99]
	global_load_dword v250, v[248:249], off
	v_lshl_add_u64 v[248:249], v[248:249], 0, s[98:99]
	global_load_dword v250, v[248:249], off
	v_lshl_add_u64 v[248:249], v[248:249], 0, s[98:99]
	global_load_dword v250, v[248:249], off
	v_lshl_add_u64 v[248:249], v[248:249], 0, s[98:99]
	global_load_dword v250, v[248:249], off
	v_lshl_add_u64 v[248:249], v[248:249], 0, s[98:99]
	global_load_dword v250, v[248:249], off
	v_lshl_add_u64 v[248:249], v[248:249], 0, s[98:99]
	global_load_dword v250, v[248:249], off
	v_lshl_add_u64 v[248:249], v[248:249], 0, s[98:99]
	global_load_dword v250, v[248:249], off
	v_lshl_add_u64 v[248:249], v[248:249], 0, s[98:99]
	global_load_dword v250, v[248:249], off
	v_lshl_add_u64 v[248:249], v[248:249], 0, s[98:99]
	global_load_dword v250, v[248:249], off
	v_lshl_add_u64 v[248:249], v[248:249], 0, s[98:99]
	global_load_dword v250, v[248:249], off
	v_lshl_add_u64 v[248:249], v[248:249], 0, s[98:99]
	global_load_dword v250, v[248:249], off
	v_lshl_add_u64 v[248:249], v[248:249], 0, s[98:99]
	global_load_dword v250, v[248:249], off
	v_lshl_add_u64 v[248:249], v[248:249], 0, s[98:99]
	global_load_dword v250, v[248:249], off
	v_lshl_add_u64 v[248:249], v[248:249], 0, s[98:99]
	global_load_dword v250, v[248:249], off
	v_lshl_add_u64 v[248:249], v[248:249], 0, s[98:99]
	global_load_dword v250, v[248:249], off
	v_lshl_add_u64 v[248:249], v[248:249], 0, s[98:99]
	global_load_dword v250, v[248:249], off
	v_lshl_add_u64 v[248:249], v[248:249], 0, s[98:99]
	global_load_dword v250, v[248:249], off
	v_lshl_add_u64 v[248:249], v[248:249], 0, s[98:99]
	global_load_dword v250, v[248:249], off
	v_lshl_add_u64 v[248:249], v[248:249], 0, s[98:99]
	global_load_dword v250, v[248:249], off
	v_lshl_add_u64 v[248:249], v[248:249], 0, s[98:99]
	global_load_dword v250, v[248:249], off
	v_lshl_add_u64 v[248:249], v[248:249], 0, s[98:99]
	global_load_dword v250, v[248:249], off
	v_lshl_add_u64 v[248:249], v[248:249], 0, s[98:99]
	global_load_dword v250, v[248:249], off
	v_lshl_add_u64 v[248:249], v[248:249], 0, s[98:99]
	global_load_dword v250, v[248:249], off
	v_lshl_add_u64 v[248:249], v[248:249], 0, s[98:99]
	global_load_dword v250, v[248:249], off
	v_lshl_add_u64 v[248:249], v[248:249], 0, s[98:99]
	global_load_dword v250, v[248:249], off
	v_lshl_add_u64 v[248:249], v[248:249], 0, s[98:99]
	global_load_dword v250, v[248:249], off
	v_lshl_add_u64 v[248:249], v[248:249], 0, s[98:99]
	global_load_dword v250, v[248:249], off
	v_lshl_add_u64 v[248:249], v[248:249], 0, s[98:99]
	global_load_dword v250, v[248:249], off
	v_lshl_add_u64 v[248:249], v[248:249], 0, s[98:99]
	global_load_dword v250, v[248:249], off
	v_lshl_add_u64 v[248:249], v[248:249], 0, s[98:99]
	global_load_dword v250, v[248:249], off
	v_lshl_add_u64 v[248:249], v[248:249], 0, s[98:99]
	global_load_dword v250, v[248:249], off
	v_lshl_add_u64 v[248:249], v[248:249], 0, s[98:99]
	global_load_dword v250, v[248:249], off
	v_lshl_add_u64 v[248:249], v[248:249], 0, s[98:99]
	global_load_dword v250, v[248:249], off
	v_lshl_add_u64 v[248:249], v[248:249], 0, s[98:99]
	global_load_dword v250, v[248:249], off
	v_lshl_add_u64 v[248:249], v[248:249], 0, s[98:99]
	global_load_dword v250, v[248:249], off
	v_lshl_add_u64 v[248:249], v[248:249], 0, s[98:99]
	global_load_dword v250, v[248:249], off
	v_lshl_add_u64 v[248:249], v[248:249], 0, s[98:99]
	global_load_dword v250, v[248:249], off
	v_lshl_add_u64 v[248:249], v[248:249], 0, s[98:99]
	global_load_dword v250, v[248:249], off
	v_lshl_add_u64 v[248:249], v[248:249], 0, s[98:99]
	global_load_dword v250, v[248:249], off
	v_lshl_add_u64 v[248:249], v[248:249], 0, s[98:99]
	global_load_dword v250, v[248:249], off
	v_lshl_add_u64 v[248:249], v[248:249], 0, s[98:99]
	global_load_dword v250, v[248:249], off
	v_lshl_add_u64 v[248:249], v[248:249], 0, s[98:99]
	global_load_dword v250, v[248:249], off
	v_lshl_add_u64 v[248:249], v[248:249], 0, s[98:99]
	global_load_dword v250, v[248:249], off
	v_lshl_add_u64 v[248:249], v[248:249], 0, s[98:99]
	global_load_dword v250, v[248:249], off
	v_lshl_add_u64 v[248:249], v[248:249], 0, s[98:99]
	global_load_dword v250, v[248:249], off
	v_lshl_add_u64 v[248:249], v[248:249], 0, s[98:99]
	global_load_dword v250, v[248:249], off
	v_lshl_add_u64 v[248:249], v[248:249], 0, s[98:99]
	global_load_dword v250, v[248:249], off
	v_lshl_add_u64 v[248:249], v[248:249], 0, s[98:99]
	global_load_dword v250, v[248:249], off
	v_lshl_add_u64 v[248:249], v[248:249], 0, s[98:99]
	global_load_dword v250, v[248:249], off
	v_lshl_add_u64 v[248:249], v[248:249], 0, s[98:99]
	global_load_dword v250, v[248:249], off
	v_lshl_add_u64 v[248:249], v[248:249], 0, s[98:99]
	global_load_dword v250, v[248:249], off
	v_lshl_add_u64 v[248:249], v[248:249], 0, s[98:99]
	global_load_dword v250, v[248:249], off
	v_lshl_add_u64 v[248:249], v[248:249], 0, s[98:99]
	global_load_dword v250, v[248:249], off
